# baseline (speedup 1.0000x reference)
_Z7k_fusedPKfS0_S0_S0_S0_S0_S0_S0_S0_S0_S0_S0_S0_S0_PfS1_:
	s_load_dwordx2 s[34:35], s[0:1], 0x70
	s_load_dwordx16 s[64:79], s[0:1], 0x0
	s_load_dwordx16 s[80:95], s[0:1], 0x40
	s_load_dwordx4 s[20:23], s[0:1], 0x60
	s_load_dwordx4 s[24:27], s[0:1], 0x40
	s_load_dwordx4 s[28:31], s[0:1], 0x10
	s_and_b32 s33, s2, 7
	s_ashr_i32 s36, s2, 3
	s_cmp_lt_i32 s36, 31
	s_mov_b64 s[2:3], -1
	s_cbranch_scc1 .LBB5_52
	s_endpgm
	s_mul_i32 s11, s33, 0x1cc8
	v_add_u32_e32 v1, s11, v0
	v_lshlrev_b32_e32 v22, 4, v1
	v_mov_b32_e32 v23, 0
	s_add_i32 s8, s11, 0x1cc8
	s_add_i32 s9, s11, 0x1a48
	s_add_i32 s10, s11, 0x17c8
	s_addk_i32 s11, 0x1548
	s_waitcnt lgkmcnt(0)
	v_lshl_add_u64 v[24:25], s[28:29], 0, v[22:23]
	s_mov_b64 s[2:3], 0
	s_mov_b64 s[4:5], 0xa000
	v_mov_b32_e32 v26, v1
	v_mov_b32_e32 v18, v23
	v_mov_b32_e32 v19, v23
	v_mov_b32_e32 v20, v23
	v_mov_b32_e32 v21, v23
	s_branch .LBB5_3

.LBB5_55:
	s_load_dwordx8 s[12:19], s[2:3], 0x4
	s_load_dword s49, s[2:3], 0x24
	s_add_u32 s42, s34, 0x125000
	s_addc_u32 s43, s35, 0
	v_lshlrev_b32_e32 v78, 4, v0
	global_load_dwordx4 v[2:5], v78, s[42:43]
	s_mov_b64 s[4:5], s[74:75]
	v_mov_b32_e32 v79, 0
	s_movk_i32 s6, 0x80
	v_lshl_add_u64 v[84:85], s[42:43], 0, v[78:79]
	v_cmp_gt_u32_e64 s[10:11], s6, v0
	s_and_saveexec_b64 s[6:7], s[10:11]
	s_cbranch_execz .LBB5_57
	v_add_co_u32_e32 v6, vcc, 0x2000, v84
	s_nop 1
	v_addc_co_u32_e32 v7, vcc, 0, v85, vcc
	global_load_dwordx4 v[6:9], v[6:7], off offset:2048

.LBB5_61:
	s_or_saveexec_b64 s[6:7], s[6:7]
	v_mov_b64_e32 v[10:11], s[4:5]
	v_lshlrev_b32_e32 v12, 2, v0
	s_xor_b64 exec, exec, s[6:7]
	s_cbranch_execz .LBB5_63
	s_mov_b64 s[4:5], s[66:67]
	s_mov_b64 s[38:39], s[72:73]
	global_load_dword v1, v12, s[4:5]
	v_mov_b64_e32 v[10:11], s[38:39]
.LBB5_63:
	s_or_b64 exec, exec, s[6:7]
	s_movk_i32 s4, 0xff
	v_cmp_lt_u32_e32 vcc, s4, v0
	s_movk_i32 s4, 0x100
	v_and_b32_e32 v128, 63, v0
	v_cmp_gt_u32_e64 s[4:5], s4, v0
	v_mov_b32_e32 v14, 0
	s_and_saveexec_b64 s[38:39], s[4:5]
	s_cbranch_execz .LBB5_65
	s_mov_b64 s[52:53], s[76:77]
	s_mov_b64 s[54:55], s[78:79]
	s_movk_i32 s6, 0xc0
	v_cmp_gt_u32_e64 s[6:7], s6, v0
	v_mov_b32_e32 v13, s54
	v_mov_b32_e32 v14, s52
	v_mov_b32_e32 v15, s55
	v_cndmask_b32_e64 v13, v13, v14, s[6:7]
	v_mov_b32_e32 v14, s53
	v_cndmask_b32_e64 v14, v15, v14, s[6:7]
	v_cndmask_b32_e64 v11, v14, v11, s[10:11]
	v_cndmask_b32_e64 v10, v13, v10, s[10:11]
	v_lshlrev_b32_e32 v14, 2, v128
	v_mov_b32_e32 v15, 0
	v_lshl_add_u64 v[10:11], v[10:11], 0, v[14:15]
	global_load_dword v14, v[10:11], off
.LBB5_65:
	s_or_b64 exec, exec, s[38:39]
	s_and_saveexec_b64 s[2:3], vcc
	s_xor_b64 s[2:3], exec, s[2:3]
	s_cbranch_execz .LBB5_69
	s_movk_i32 s6, 0x140
	v_cmp_gt_u32_e32 vcc, s6, v0
	v_mov_b32_e32 v15, 0
	s_and_saveexec_b64 s[6:7], vcc
	s_cbranch_execz .LBB5_68
	s_mov_b64 s[38:39], s[86:87]
	global_load_dword v15, v12, s[38:39] offset:-1024
.LBB5_68:
	s_or_b64 exec, exec, s[6:7]
	s_or_saveexec_b64 s[2:3], s[2:3]
	s_mov_b64 s[6:7], s[64:65]
	s_xor_b64 exec, exec, s[2:3]
	s_cbranch_execnz .LBB5_70
	s_branch .LBB5_71
.LBB5_69:
	s_or_saveexec_b64 s[2:3], s[2:3]
	s_mov_b64 s[6:7], s[64:65]
	s_xor_b64 exec, exec, s[2:3]
	s_cbranch_execz .LBB5_71
.LBB5_70:
	s_mov_b64 s[38:39], s[84:85]
	global_load_dword v15, v12, s[38:39]

.LBB5_83:
	s_or_b64 exec, exec, s[12:13]
	s_mov_b64 s[40:41], s[94:95]
	v_lshrrev_b32_e32 v126, 4, v128
	v_and_b32_e32 v127, 15, v0
	s_waitcnt vmcnt(12)
	v_mul_u32_u24_e32 v1, 48, v126
	s_waitcnt lgkmcnt(0)
	s_barrier
	v_or_b32_e32 v129, v1, v127
	s_mul_i32 s46, s45, 0xc00
	v_cmp_gt_u32_e64 s[2:3], 12, v127
	v_cndmask_b32_e64 v1, 0, 1, s[8:9]
	v_lshlrev_b32_e32 v131, 2, v126
	s_add_i32 s46, s46, 0x1b000
	v_mov_b32_e32 v71, 0
	v_cndmask_b32_e64 v130, 0, 1.0, s[2:3]
	v_cmp_ne_u32_e64 s[0:1], 1, v1
	s_andn2_b64 vcc, exec, s[8:9]
	v_add_u32_e32 v79, -8, v129
	v_mov_b32_e32 v70, 0
	s_cbranch_vccnz .Lmy_inact93
	v_cndmask_b32_e64 v1, v79, v129, s[2:3]
	v_lshlrev_b32_e32 v81, 2, v1
	v_add_u32_e32 v1, 0x22800, v81
	ds_read2_b32 v[6:7], v1 offset1:12
	ds_read2_b32 v[8:9], v1 offset0:24 offset1:36
	ds_read2_b32 v[10:11], v1 offset0:192 offset1:204
	ds_read2_b32 v[12:13], v1 offset0:216 offset1:228
	v_add_u32_e32 v2, 0x400, v1
	v_add_u32_e32 v1, 0x800, v1
	ds_read2_b32 v[14:15], v2 offset0:128 offset1:140
	ds_read2_b32 v[16:17], v2 offset0:152 offset1:164
	ds_read2_b32 v[70:71], v1 offset0:64 offset1:76
	ds_read_b128 v[2:5], v80
	ds_read2_b32 v[72:73], v1 offset0:88 offset1:100
	s_waitcnt lgkmcnt(0)
	v_cvt_pk_bf16_f32 v18, v6, v7
	v_cvt_pk_bf16_f32 v19, v8, v9
	ds_read_b128 v[6:9], v80 offset:1024
	v_cvt_pk_bf16_f32 v20, v10, v11
	v_cvt_pk_bf16_f32 v21, v12, v13
	ds_read_b128 v[10:13], v80 offset:2048
	v_cvt_pk_bf16_f32 v86, v14, v15
	v_mfma_f32_16x16x32_bf16 v[2:5], v[2:5], v[18:21], 0
	v_cvt_pk_bf16_f32 v87, v16, v17
	v_cvt_pk_bf16_f32 v88, v70, v71
	v_cvt_pk_bf16_f32 v89, v72, v73
	ds_read_b128 v[70:73], v80 offset:4096
	v_mov_b32_e32 v1, 0x23e00
	s_waitcnt lgkmcnt(2)
	v_mfma_f32_16x16x32_bf16 v[14:17], v[6:9], v[86:89], v[2:5]
	v_add_u32_e32 v96, s46, v81
	s_cmp_lt_i32 s48, 1
	ds_read_b128 v[74:77], v80 offset:6144
	ds_read_b128 v[2:5], v80 offset:3072
	s_waitcnt lgkmcnt(3)
	v_mfma_f32_16x16x32_bf16 v[6:9], v[10:13], v[18:21], 0
	s_mov_b32 s8, 0x43998000
	s_waitcnt lgkmcnt(0)
	v_mfma_f32_16x16x32_bf16 v[10:13], v[2:5], v[86:89], v[6:9]
	ds_read_b128 v[2:5], v80 offset:5120
	v_mfma_f32_16x16x32_bf16 v[6:9], v[70:73], v[18:21], 0
	ds_read_b128 v[70:73], v80 offset:7168
	s_waitcnt lgkmcnt(1)
	v_mfma_f32_16x16x32_bf16 v[6:9], v[2:5], v[86:89], v[6:9]
	v_mfma_f32_16x16x32_bf16 v[2:5], v[74:77], v[18:21], 0
	v_mov_b32_e32 v18, 0x23e10
	ds_read_b128 v[98:101], v1
	ds_read_b128 v[18:21], v18
	v_add_u32_e32 v1, s46, v80
	s_waitcnt vmcnt(11)
	ds_write_b128 v1, v[22:25]
	s_waitcnt vmcnt(10)
	ds_write_b128 v1, v[62:65] offset:1024
	s_waitcnt vmcnt(9)
	ds_write_b128 v1, v[66:69] offset:2048
	s_waitcnt lgkmcnt(5)
	v_mfma_f32_16x16x32_bf16 v[2:5], v[70:73], v[86:89], v[2:5]
	ds_read2_b32 v[88:89], v96 offset1:12
	ds_read2_b32 v[90:91], v96 offset0:24 offset1:36
	ds_read2_b32 v[86:87], v96 offset0:192 offset1:204
	ds_read2_b32 v[82:83], v96 offset0:216 offset1:228
	v_add_u32_e32 v63, 0x400, v96
	ds_read2_b32 v[66:67], v63 offset0:128 offset1:140
	ds_read2_b32 v[68:69], v63 offset0:152 offset1:164
	v_add_u32_e32 v62, 0x800, v96
	ds_read_b128 v[22:25], v80 offset:8192
	ds_read2_b32 v[94:95], v62 offset0:64 offset1:76
	ds_read2_b32 v[92:93], v62 offset0:88 offset1:100
	ds_read_b128 v[106:109], v80 offset:9216
	s_waitcnt lgkmcnt(9)
	v_cvt_pk_bf16_f32 v102, v88, v89
	s_waitcnt lgkmcnt(8)
	v_cvt_pk_bf16_f32 v103, v90, v91
	s_waitcnt lgkmcnt(7)
	v_cvt_pk_bf16_f32 v104, v86, v87
	s_waitcnt lgkmcnt(6)
	v_cvt_pk_bf16_f32 v105, v82, v83
	s_waitcnt lgkmcnt(5)
	v_cvt_pk_bf16_f32 v110, v66, v67
	s_waitcnt lgkmcnt(4)
	v_cvt_pk_bf16_f32 v111, v68, v69
	s_waitcnt lgkmcnt(3)
	v_mfma_f32_16x16x32_bf16 v[22:25], v[22:25], v[102:105], v[98:101]
	s_waitcnt lgkmcnt(2)
	v_cvt_pk_bf16_f32 v112, v94, v95
	s_waitcnt lgkmcnt(1)
	v_cvt_pk_bf16_f32 v113, v92, v93
	s_waitcnt lgkmcnt(0)
	s_nop 0
	v_mfma_f32_16x16x32_bf16 v[22:25], v[106:109], v[110:113], v[22:25]
	s_mul_i32 s58, s37, 0xc00
	v_add_u32_e32 v133, s58, v80
	global_load_dwordx4 v[136:139], v133, s[28:29]
	global_load_dwordx4 v[140:143], v133, s[28:29] offset:1024
	global_load_dwordx4 v[144:147], v133, s[28:29] offset:2048
	global_load_dwordx4 v[148:151], v133, s[30:31]
	global_load_dwordx4 v[156:159], v133, s[30:31] offset:1024
	global_load_dwordx4 v[160:163], v133, s[30:31] offset:2048
	s_cbranch_scc1 .LBB5_209
	s_waitcnt vmcnt(14)
	ds_write_b128 v1, v[50:53]
	s_waitcnt vmcnt(13)
	ds_write_b128 v1, v[54:57] offset:1024
	s_waitcnt vmcnt(12)
	ds_write_b128 v1, v[58:61] offset:2048
	ds_read2_b32 v[54:55], v96 offset1:12
	ds_read2_b32 v[56:57], v96 offset0:24 offset1:36
	ds_read2_b32 v[64:65], v96 offset0:192 offset1:204
	ds_read2_b32 v[98:99], v96 offset0:216 offset1:228
	ds_read2_b32 v[100:101], v63 offset0:128 offset1:140
	ds_read2_b32 v[102:103], v63 offset0:152 offset1:164
	ds_read2_b32 v[104:105], v62 offset0:64 offset1:76
	ds_read_b128 v[50:53], v80
	ds_read2_b32 v[106:107], v62 offset0:88 offset1:100
	ds_read_b128 v[58:61], v80 offset:1024
	s_waitcnt lgkmcnt(9)
	v_cvt_pk_bf16_f32 v54, v54, v55
	s_waitcnt lgkmcnt(8)
	v_cvt_pk_bf16_f32 v55, v56, v57
	s_waitcnt lgkmcnt(7)
	v_cvt_pk_bf16_f32 v56, v64, v65
	s_waitcnt lgkmcnt(6)
	v_cvt_pk_bf16_f32 v57, v98, v99
	s_waitcnt lgkmcnt(5)
	v_cvt_pk_bf16_f32 v62, v100, v101
	ds_read_b128 v[98:101], v80 offset:2048
	s_waitcnt lgkmcnt(3)
	v_mfma_f32_16x16x32_bf16 v[50:53], v[50:53], v[54:57], 0
	v_cvt_pk_bf16_f32 v63, v102, v103
	v_cvt_pk_bf16_f32 v64, v104, v105
	s_waitcnt lgkmcnt(2)
	v_cvt_pk_bf16_f32 v65, v106, v107
	s_waitcnt lgkmcnt(0)
	v_mfma_f32_16x16x32_bf16 v[98:101], v[98:101], v[54:57], 0
	ds_read_b128 v[102:105], v80 offset:4096
	ds_read_b128 v[106:109], v80 offset:11264
	v_mfma_f32_16x16x32_bf16 v[50:53], v[58:61], v[62:65], v[50:53]
	ds_read_b128 v[58:61], v80 offset:3072
	s_waitcnt lgkmcnt(0)
	v_mfma_f32_16x16x32_bf16 v[58:61], v[58:61], v[62:65], v[98:101]
	s_nop 2
	ds_read_b128 v[98:101], v80 offset:5120
	v_mfma_f32_16x16x32_bf16 v[102:105], v[102:105], v[54:57], 0
	s_waitcnt lgkmcnt(0)
	v_mfma_f32_16x16x32_bf16 v[98:101], v[98:101], v[62:65], v[102:105]
	s_nop 5
	ds_read_b128 v[102:105], v80 offset:10240
	v_mfma_f32_16x16x32_bf16 v[74:77], v[74:77], v[54:57], 0
	s_waitcnt lgkmcnt(0)
	v_mfma_f32_16x16x32_bf16 v[54:57], v[102:105], v[54:57], v[18:21]
	v_mfma_f32_16x16x32_bf16 v[54:57], v[106:109], v[62:65], v[54:57]
	v_mfma_f32_16x16x32_bf16 v[62:65], v[70:73], v[62:65], v[74:77]
	s_nop 6
	v_add_f32_e32 v54, v22, v54
	v_mul_f32_e32 v81, 0x3e4ccccd, v54
	v_cmp_lt_f32_e32 vcc, 0, v54
	v_add_f32_e32 v55, v23, v55
	v_mul_f32_e32 v97, 0x3e4ccccd, v55
	v_cndmask_b32_e32 v54, v81, v54, vcc
	v_cmp_lt_f32_e32 vcc, 0, v55
	v_mov_b32_e32 v81, s18
	v_fma_f32 v54, s15, v54, v81
	v_cndmask_b32_e32 v55, v97, v55, vcc
	v_fma_f32 v55, s15, v55, v81
	v_mul_f32_e32 v54, 0x3fb8aa3b, v54
	v_mul_f32_e32 v55, 0x3fb8aa3b, v55
	v_exp_f32_e32 v54, v54
	v_exp_f32_e32 v55, v55
	s_nop 0
	v_pk_add_f32 v[54:55], v[54:55], -1.0 op_sel_hi:[1,0]
	s_nop 0
	v_pk_fma_f32 v[16:17], v[52:53], v[54:55], v[16:17] op_sel_hi:[1,0,1]
	v_add_f32_e32 v52, v24, v56
	v_mul_f32_e32 v53, 0x3e4ccccd, v52
	v_cmp_lt_f32_e32 vcc, 0, v52
	v_pk_fma_f32 v[14:15], v[50:51], v[54:55], v[14:15] op_sel_hi:[1,0,1]
	v_pk_fma_f32 v[12:13], v[60:61], v[54:55], v[12:13] op_sel:[0,1,0]
	v_cndmask_b32_e32 v52, v53, v52, vcc
	v_add_f32_e32 v53, v25, v57
	v_mul_f32_e32 v56, 0x3e4ccccd, v53
	v_cmp_lt_f32_e32 vcc, 0, v53
	v_fma_f32 v52, s15, v52, v81
	v_mul_f32_e32 v52, 0x3fb8aa3b, v52
	v_cndmask_b32_e32 v53, v56, v53, vcc
	v_fma_f32 v53, s15, v53, v81
	v_mul_f32_e32 v53, 0x3fb8aa3b, v53
	v_exp_f32_e32 v52, v52
	v_exp_f32_e32 v53, v53
	v_pk_fma_f32 v[10:11], v[58:59], v[54:55], v[10:11] op_sel:[0,1,0]
	v_pk_add_f32 v[72:73], v[54:55], s[8:9] op_sel_hi:[1,0]
	v_pk_add_f32 v[50:51], v[52:53], -1.0 op_sel_hi:[1,0]
	s_nop 0
	v_pk_fma_f32 v[8:9], v[100:101], v[50:51], v[8:9] op_sel_hi:[1,0,1]
	v_pk_fma_f32 v[6:7], v[98:99], v[50:51], v[6:7] op_sel_hi:[1,0,1]
	v_pk_add_f32 v[70:71], v[50:51], s[8:9] op_sel_hi:[1,0]
	v_pk_fma_f32 v[4:5], v[64:65], v[50:51], v[4:5] op_sel:[0,1,0]
	v_pk_fma_f32 v[2:3], v[62:63], v[50:51], v[2:3] op_sel:[0,1,0]
	s_cmp_lt_i32 s48, 2
	s_cbranch_scc1 .LBB5_87

amdhsa.kernels:
  - .agpr_count:     0
    .args:
      - .actual_access:  read_only
        .address_space:  global
        .offset:         0
        .size:           8
        .value_kind:     global_buffer
      - .actual_access:  read_only
        .address_space:  global
        .offset:         8
        .size:           8
        .value_kind:     global_buffer
      - .actual_access:  read_only
        .address_space:  global
        .offset:         16
        .size:           8
        .value_kind:     global_buffer
      - .actual_access:  read_only
        .address_space:  global
        .offset:         24
        .size:           8
        .value_kind:     global_buffer
      - .actual_access:  read_only
        .address_space:  global
        .offset:         32
        .size:           8
        .value_kind:     global_buffer
      - .actual_access:  read_only
        .address_space:  global
        .offset:         40
        .size:           8
        .value_kind:     global_buffer
      - .actual_access:  read_only
        .address_space:  global
        .offset:         48
        .size:           8
        .value_kind:     global_buffer
      - .actual_access:  read_only
        .address_space:  global
        .offset:         56
        .size:           8
        .value_kind:     global_buffer
      - .actual_access:  read_only
        .address_space:  global
        .offset:         64
        .size:           8
        .value_kind:     global_buffer
      - .actual_access:  read_only
        .address_space:  global
        .offset:         72
        .size:           8
        .value_kind:     global_buffer
      - .actual_access:  read_only
        .address_space:  global
        .offset:         80
        .size:           8
        .value_kind:     global_buffer
      - .actual_access:  read_only
        .address_space:  global
        .offset:         88
        .size:           8
        .value_kind:     global_buffer
      - .actual_access:  read_only
        .address_space:  global
        .offset:         96
        .size:           8
        .value_kind:     global_buffer
      - .actual_access:  write_only
        .address_space:  global
        .offset:         104
        .size:           8
        .value_kind:     global_buffer
    .group_segment_fixed_size: 1024
    .kernarg_segment_align: 8
    .kernarg_segment_size: 112
    .language:       OpenCL C
    .language_version:
      - 2
      - 0
    .max_flat_workgroup_size: 256
    .name:           _Z7k0_prepPKfS0_S0_S0_S0_S0_S0_S0_S0_S0_S0_S0_S0_Pf
    .private_segment_fixed_size: 0
    .sgpr_count:     36
    .sgpr_spill_count: 0
    .symbol:         _Z7k0_prepPKfS0_S0_S0_S0_S0_S0_S0_S0_S0_S0_S0_S0_Pf.kd
    .uniform_work_group_size: 1
    .uses_dynamic_stack: false
    .vgpr_count:     58
    .vgpr_spill_count: 0
    .wavefront_size: 64
  - .agpr_count:     0
    .args:
      - .actual_access:  read_only
        .address_space:  global
        .offset:         0
        .size:           8
        .value_kind:     global_buffer
      - .actual_access:  read_only
        .address_space:  global
        .offset:         8
        .size:           8
        .value_kind:     global_buffer
      - .address_space:  global
        .offset:         16
        .size:           8
        .value_kind:     global_buffer
      - .actual_access:  write_only
        .address_space:  global
        .offset:         24
        .size:           8
        .value_kind:     global_buffer
    .group_segment_fixed_size: 46400
    .kernarg_segment_align: 8
    .kernarg_segment_size: 32
    .language:       OpenCL C
    .language_version:
      - 2
      - 0
    .max_flat_workgroup_size: 640
    .name:           _Z6k1_gatPKfS0_PfS1_
    .private_segment_fixed_size: 0
    .sgpr_count:     38
    .sgpr_spill_count: 0
    .symbol:         _Z6k1_gatPKfS0_PfS1_.kd
    .uniform_work_group_size: 1
    .uses_dynamic_stack: false
    .vgpr_count:     124
    .vgpr_spill_count: 0
    .wavefront_size: 64
  - .agpr_count:     0
    .args:
      - .actual_access:  read_only
        .address_space:  global
        .offset:         0
        .size:           8
        .value_kind:     global_buffer
      - .actual_access:  read_only
        .address_space:  global
        .offset:         8
        .size:           8
        .value_kind:     global_buffer
      - .actual_access:  read_only
        .address_space:  global
        .offset:         16
        .size:           8
        .value_kind:     global_buffer
      - .actual_access:  read_only
        .address_space:  global
        .offset:         24
        .size:           8
        .value_kind:     global_buffer
      - .actual_access:  read_only
        .address_space:  global
        .offset:         32
        .size:           8
        .value_kind:     global_buffer
      - .actual_access:  read_only
        .address_space:  global
        .offset:         40
        .size:           8
        .value_kind:     global_buffer
      - .address_space:  global
        .offset:         48
        .size:           8
        .value_kind:     global_buffer
      - .address_space:  global
        .offset:         56
        .size:           8
        .value_kind:     global_buffer
    .group_segment_fixed_size: 64528
    .kernarg_segment_align: 8
    .kernarg_segment_size: 64
    .language:       OpenCL C
    .language_version:
      - 2
      - 0
    .max_flat_workgroup_size: 640
    .name:           _Z7k2_attnPKfS0_S0_S0_S0_S0_PfS1_
    .private_segment_fixed_size: 0
    .sgpr_count:     34
    .sgpr_spill_count: 0
    .symbol:         _Z7k2_attnPKfS0_S0_S0_S0_S0_PfS1_.kd
    .uniform_work_group_size: 1
    .uses_dynamic_stack: false
    .vgpr_count:     102
    .vgpr_spill_count: 0
    .wavefront_size: 64
  - .agpr_count:     0
    .args:
      - .actual_access:  read_only
        .address_space:  global
        .offset:         0
        .size:           8
        .value_kind:     global_buffer
      - .actual_access:  read_only
        .address_space:  global
        .offset:         8
        .size:           8
        .value_kind:     global_buffer
      - .actual_access:  read_only
        .address_space:  global
        .offset:         16
        .size:           8
        .value_kind:     global_buffer
      - .actual_access:  read_only
        .address_space:  global
        .offset:         24
        .size:           8
        .value_kind:     global_buffer
      - .address_space:  global
        .offset:         32
        .size:           8
        .value_kind:     global_buffer
      - .address_space:  global
        .offset:         40
        .size:           8
        .value_kind:     global_buffer
    .group_segment_fixed_size: 97552
    .kernarg_segment_align: 8
    .kernarg_segment_size: 48
    .language:       OpenCL C
    .language_version:
      - 2
      - 0
    .max_flat_workgroup_size: 640
    .name:           _Z5k3_ffPKfS0_S0_S0_PfS1_
    .private_segment_fixed_size: 0
    .sgpr_count:     29
    .sgpr_spill_count: 0
    .symbol:         _Z5k3_ffPKfS0_S0_S0_PfS1_.kd
    .uniform_work_group_size: 1
    .uses_dynamic_stack: false
    .vgpr_count:     88
    .vgpr_spill_count: 0
    .wavefront_size: 64
  - .agpr_count:     0
    .args:
      - .actual_access:  read_only
        .address_space:  global
        .offset:         0
        .size:           8
        .value_kind:     global_buffer
      - .actual_access:  read_only
        .address_space:  global
        .offset:         8
        .size:           8
        .value_kind:     global_buffer
      - .actual_access:  read_only
        .address_space:  global
        .offset:         16
        .size:           8
        .value_kind:     global_buffer
      - .address_space:  global
        .offset:         24
        .size:           8
        .value_kind:     global_buffer
    .group_segment_fixed_size: 8
    .kernarg_segment_align: 8
    .kernarg_segment_size: 32
    .language:       OpenCL C
    .language_version:
      - 2
      - 0
    .max_flat_workgroup_size: 640
    .name:           _Z6k4_ln3PKfS0_S0_Pf
    .private_segment_fixed_size: 0
    .sgpr_count:     21
    .sgpr_spill_count: 0
    .symbol:         _Z6k4_ln3PKfS0_S0_Pf.kd
    .uniform_work_group_size: 1
    .uses_dynamic_stack: false
    .vgpr_count:     50
    .vgpr_spill_count: 0
    .wavefront_size: 64
  - .agpr_count:     0
    .args:
      - .actual_access:  read_only
        .address_space:  global
        .offset:         0
        .size:           8
        .value_kind:     global_buffer
      - .actual_access:  read_only
        .address_space:  global
        .offset:         8
        .size:           8
        .value_kind:     global_buffer
      - .actual_access:  read_only
        .address_space:  global
        .offset:         16
        .size:           8
        .value_kind:     global_buffer
      - .actual_access:  read_only
        .address_space:  global
        .offset:         24
        .size:           8
        .value_kind:     global_buffer
      - .actual_access:  read_only
        .address_space:  global
        .offset:         32
        .size:           8
        .value_kind:     global_buffer
      - .actual_access:  read_only
        .address_space:  global
        .offset:         40
        .size:           8
        .value_kind:     global_buffer
      - .actual_access:  read_only
        .address_space:  global
        .offset:         48
        .size:           8
        .value_kind:     global_buffer
      - .actual_access:  read_only
        .address_space:  global
        .offset:         56
        .size:           8
        .value_kind:     global_buffer
      - .actual_access:  read_only
        .address_space:  global
        .offset:         64
        .size:           8
        .value_kind:     global_buffer
      - .actual_access:  read_only
        .address_space:  global
        .offset:         72
        .size:           8
        .value_kind:     global_buffer
      - .actual_access:  read_only
        .address_space:  global
        .offset:         80
        .size:           8
        .value_kind:     global_buffer
      - .actual_access:  read_only
        .address_space:  global
        .offset:         88
        .size:           8
        .value_kind:     global_buffer
      - .actual_access:  read_only
        .address_space:  global
        .offset:         96
        .size:           8
        .value_kind:     global_buffer
      - .actual_access:  read_only
        .address_space:  global
        .offset:         104
        .size:           8
        .value_kind:     global_buffer
      - .address_space:  global
        .offset:         112
        .size:           8
        .value_kind:     global_buffer
      - .actual_access:  write_only
        .address_space:  global
        .offset:         120
        .size:           8
        .value_kind:     global_buffer
    .group_segment_fixed_size: 147104
    .kernarg_segment_align: 8
    .kernarg_segment_size: 128
    .language:       OpenCL C
    .language_version:
      - 2
      - 0
    .max_flat_workgroup_size: 640
    .name:           _Z7k_fusedPKfS0_S0_S0_S0_S0_S0_S0_S0_S0_S0_S0_S0_S0_PfS1_
    .private_segment_fixed_size: 0
    .sgpr_count:     102
    .sgpr_spill_count: 0
    .symbol:         _Z7k_fusedPKfS0_S0_S0_S0_S0_S0_S0_S0_S0_S0_S0_S0_S0_PfS1_.kd
    .uniform_work_group_size: 1
    .uses_dynamic_stack: false
    .vgpr_count:     168
    .vgpr_spill_count: 0
    .wavefront_size: 64
